# speedup vs baseline: 1.0254x; 1.0254x over previous
.Lu2w_done:
	s_barrier
	s_lshr_b32 s26, s23, 6
	s_mov_b32 s5, 0
	s_add_i32 s27, s27, 0x18000
	v_mov_b32_e32 v15, 0
	v_cmp_neq_f32_e64 s[2:3], 0, v192
	s_andn2_b64 vcc, exec, s[16:17]
	s_mov_b32 s18, 1
	s_cbranch_vccnz .LBB1_86
	s_cmp_eq_u64 s[2:3], 0
	s_cselect_b64 s[2:3], -1, 0
	s_lshl_b32 s4, s26, 2
	s_and_b32 s4, s4, 4
	s_lshl_b32 s19, s25, 14
	s_lshl_b32 s29, s26, 10
	s_cmp_lg_u32 0, -1
	v_bitop3_b32 v0, s4, v200, v208 bitop3:0x36
	s_cselect_b32 s4, 0, 0
	v_lshl_or_b32 v48, s26, 3, v193
	v_mov_b32_e32 v49, 0
	v_or_b32_e32 v4, s19, v1
	s_add_i32 s29, s29, s4
	v_lshlrev_b64 v[2:3], 11, v[48:49]
	s_add_i32 s16, s30, 0x4000
	v_lshlrev_b32_e32 v48, 1, v4
	s_lshl_b32 s4, s24, 6
	s_add_i32 s31, s29, 0xc000
	v_lshl_add_u64 v[4:5], s[14:15], 0, v[48:49]
	s_cmpk_lg_u32 s30, 0x8000
	v_lshl_add_u64 v[2:3], s[6:7], 0, v[2:3]
	v_lshl_add_u64 v[4:5], v[4:5], 0, s[4:5]
	v_lshlrev_b32_e32 v48, 4, v0
	s_cselect_b32 s35, s16, 0
	s_min_u32 s4, s33, 3
	v_lshl_add_u64 v[194:195], v[2:3], 0, v[48:49]
	s_lshl_b32 s4, s4, 18
	v_lshl_add_u64 v[2:3], v[194:195], 0, s[4:5]
	s_add_i32 s4, s29, s30
	s_mov_b32 s6, m0
	s_mov_b32 m0, s4
	s_nop 0
	global_load_lds_dwordx4 v[2:3], off
	s_mov_b32 m0, s6
	s_mov_b64 s[6:7], 0x20000
	v_mov_b32_e32 v191, v49
	v_lshl_add_u64 v[2:3], v[2:3], 0, s[6:7]
	s_addk_i32 s4, 0x2000
	s_mov_b32 s14, m0
	s_mov_b32 m0, s4
	s_nop 0
	global_load_lds_dwordx4 v[2:3], off
	s_mov_b32 m0, s14
	v_lshl_add_u64 v[190:191], v[4:5], 0, v[190:191]
	s_mov_b64 s[14:15], 0x40000
	v_lshl_add_u64 v[2:3], v[190:191], 0, s[14:15]
	s_add_i32 s4, s31, s35
	s_mov_b32 s16, m0
	s_mov_b32 m0, s4
	s_nop 0
	global_load_lds_dwordx4 v[2:3], off
	s_mov_b32 m0, s16
	s_mov_b64 s[16:17], 0x60000
	v_lshl_add_u64 v[2:3], v[190:191], 0, s[16:17]
	v_add_u32_e32 v0, s35, v199
	s_addk_i32 s4, 0x2000
	s_mov_b32 s20, m0
	s_mov_b32 m0, s4
	s_nop 0
	global_load_lds_dwordx4 v[2:3], off
	s_mov_b32 m0, s20
	v_add_u32_e32 v2, v0, v207
	ds_read_b128 v[80:83], v2
	ds_read_b128 v[96:99], v2 offset:4096
	v_add_u32_e32 v2, v0, v206
	ds_read_b128 v[164:167], v2
	ds_read_b128 v[160:163], v2 offset:4096
	v_add_u32_e32 v2, v0, v205
	v_add_u32_e32 v0, v0, v204
	ds_read_b128 v[156:159], v2
	ds_read_b128 v[152:155], v2 offset:4096
	ds_read_b128 v[148:151], v0
	ds_read_b128 v[144:147], v0 offset:4096
	s_add_i32 s4, s35, 0x4000
	s_bitcmp1_b32 s23, 8
	s_cbranch_scc1 .Lu2x_g1
	s_waitcnt vmcnt(8) lgkmcnt(0)
	s_branch .Lu2x_done

.Lu2x_done:
	s_barrier
	s_cmpk_lg_u32 s35, 0x8000
	s_cselect_b32 s28, s4, 0
	s_cmp_lt_u32 s33, 3
	s_cbranch_scc1 .LBB1_87
	s_lshr_b32 s4, s23, 2
	s_and_b32 s4, s4, 0x3fffffc0
	s_add_u32 s20, s12, s4
	s_addc_u32 s21, s13, 0
	v_lshl_add_u64 v[2:3], s[20:21], 0, v[188:189]
	v_add_lshl_u32 v48, s19, v1, 1
	s_add_u32 s8, s8, s34
	v_lshl_add_u64 v[0:1], v[2:3], 0, v[48:49]
	s_addc_u32 s9, s9, 0
	v_lshl_add_u64 v[0:1], s[8:9], 0, v[0:1]
	s_mov_b64 s[8:9], 0x80000
	v_mov_b32_e32 v48, v49
	v_lshl_add_u64 v[180:181], v[0:1], 0, s[8:9]
	v_mov_b32_e32 v50, v49
	v_mov_b32_e32 v51, v49
	v_mov_b32_e32 v52, v49
	v_mov_b32_e32 v53, v49
	v_mov_b32_e32 v54, v49
	v_mov_b32_e32 v55, v49
	v_mov_b32_e32 v56, v49
	v_mov_b32_e32 v57, v49
	v_mov_b32_e32 v58, v49
	v_mov_b32_e32 v59, v49
	v_mov_b32_e32 v60, v49
	v_mov_b32_e32 v61, v49
	v_mov_b32_e32 v62, v49
	v_mov_b32_e32 v63, v49
	v_mov_b64_e32 v[16:17], v[48:49]
	v_mov_b64_e32 v[0:1], v[48:49]
	v_lshl_add_u32 v182, v202, 2, s27
	v_lshl_add_u32 v183, v203, 2, s27
	s_mov_b32 s36, 5
	s_mov_b32 s34, 0x41000000
	v_mov_b32_e32 v184, 0xff800000
	v_mov_b64_e32 v[18:19], v[50:51]
	v_mov_b64_e32 v[20:21], v[52:53]
	v_mov_b64_e32 v[22:23], v[54:55]
	v_mov_b64_e32 v[24:25], v[56:57]
	v_mov_b64_e32 v[26:27], v[58:59]
	v_mov_b64_e32 v[28:29], v[60:61]
	v_mov_b64_e32 v[30:31], v[62:63]
	v_mov_b64_e32 v[2:3], v[50:51]
	v_mov_b64_e32 v[4:5], v[52:53]
	v_mov_b64_e32 v[6:7], v[54:55]
	v_mov_b64_e32 v[8:9], v[56:57]
	v_mov_b64_e32 v[10:11], v[58:59]
	v_mov_b64_e32 v[12:13], v[60:61]
	v_mov_b64_e32 v[14:15], v[62:63]

.LBB1_135:
	v_mov_b32_e32 v32, 0xff800000
	v_cmp_neq_f32_e32 vcc, 0, v80
	s_nop 1
	v_cndmask_b32_e32 v80, v32, v80, vcc
	v_cmp_neq_f32_e32 vcc, 0, v96
	s_nop 1
	v_cndmask_b32_e32 v96, v32, v96, vcc
	v_cmp_neq_f32_e32 vcc, 0, v81
	s_nop 1
	v_cndmask_b32_e32 v81, v32, v81, vcc
	v_cmp_neq_f32_e32 vcc, 0, v97
	s_nop 1
	v_cndmask_b32_e32 v97, v32, v97, vcc
	v_cmp_neq_f32_e32 vcc, 0, v82
	s_nop 1
	v_cndmask_b32_e32 v82, v32, v82, vcc
	v_cmp_neq_f32_e32 vcc, 0, v98
	s_nop 1
	v_cndmask_b32_e32 v98, v32, v98, vcc
	v_cmp_neq_f32_e32 vcc, 0, v83
	s_nop 1
	v_cndmask_b32_e32 v83, v32, v83, vcc
	v_cmp_neq_f32_e32 vcc, 0, v99
	s_nop 1
	v_cndmask_b32_e32 v99, v32, v99, vcc
	v_cmp_neq_f32_e32 vcc, 0, v84
	s_nop 1
	v_cndmask_b32_e32 v84, v32, v84, vcc
	v_cmp_neq_f32_e32 vcc, 0, v100
	s_nop 1
	v_cndmask_b32_e32 v100, v32, v100, vcc
	v_cmp_neq_f32_e32 vcc, 0, v85
	s_nop 1
	v_cndmask_b32_e32 v85, v32, v85, vcc
	v_cmp_neq_f32_e32 vcc, 0, v101
	s_nop 1
	v_cndmask_b32_e32 v101, v32, v101, vcc
	v_cmp_neq_f32_e32 vcc, 0, v86
	s_nop 1
	v_cndmask_b32_e32 v86, v32, v86, vcc
	v_cmp_neq_f32_e32 vcc, 0, v102
	s_nop 1
	v_cndmask_b32_e32 v102, v32, v102, vcc
	v_cmp_neq_f32_e32 vcc, 0, v87
	s_nop 1
	v_cndmask_b32_e32 v87, v32, v87, vcc
	v_cmp_neq_f32_e32 vcc, 0, v103
	s_nop 1
	v_cndmask_b32_e32 v103, v32, v103, vcc
	v_cmp_neq_f32_e32 vcc, 0, v88
	s_nop 1
	v_cndmask_b32_e32 v88, v32, v88, vcc
	v_cmp_neq_f32_e32 vcc, 0, v104
	s_nop 1
	v_cndmask_b32_e32 v104, v32, v104, vcc
	v_cmp_neq_f32_e32 vcc, 0, v89
	s_nop 1
	v_cndmask_b32_e32 v89, v32, v89, vcc
	v_cmp_neq_f32_e32 vcc, 0, v105
	s_nop 1
	v_cndmask_b32_e32 v105, v32, v105, vcc
	v_cmp_neq_f32_e32 vcc, 0, v90
	s_nop 1
	v_cndmask_b32_e32 v90, v32, v90, vcc
	v_cmp_neq_f32_e32 vcc, 0, v106
	s_nop 1
	v_cndmask_b32_e32 v106, v32, v106, vcc
	v_cmp_neq_f32_e32 vcc, 0, v91
	s_nop 1
	v_cndmask_b32_e32 v91, v32, v91, vcc
	v_cmp_neq_f32_e32 vcc, 0, v107
	s_nop 1
	v_cndmask_b32_e32 v107, v32, v107, vcc
	v_cmp_neq_f32_e32 vcc, 0, v92
	s_nop 1
	v_cndmask_b32_e32 v92, v32, v92, vcc
	v_cmp_neq_f32_e32 vcc, 0, v108
	s_nop 1
	v_cndmask_b32_e32 v108, v32, v108, vcc
	v_cmp_neq_f32_e32 vcc, 0, v93
	s_nop 1
	v_cndmask_b32_e32 v93, v32, v93, vcc
	v_cmp_neq_f32_e32 vcc, 0, v109
	s_nop 1
	v_cndmask_b32_e32 v109, v32, v109, vcc
	v_cmp_neq_f32_e32 vcc, 0, v94
	s_nop 1
	v_cndmask_b32_e32 v94, v32, v94, vcc
	v_cmp_neq_f32_e32 vcc, 0, v110
	s_nop 1
	v_cndmask_b32_e32 v110, v32, v110, vcc
	v_cmp_neq_f32_e32 vcc, 0, v95
	s_nop 1
	v_cndmask_b32_e32 v95, v32, v95, vcc
	v_cmp_neq_f32_e32 vcc, 0, v111
	s_nop 1
	v_cndmask_b32_e32 v111, v32, v111, vcc
	s_branch .LBB1_93
	s_nop 0
	s_nop 0
	s_nop 0
	s_nop 0
	s_nop 0
	s_nop 0
	s_nop 0
	s_nop 0
	s_nop 0
	s_nop 0
	s_nop 0
	s_nop 0
	s_nop 0
	s_nop 0
	s_nop 0
	s_nop 0
	s_nop 0
	s_nop 0
	s_nop 0
	s_nop 0
	s_nop 0
	s_nop 0
	s_nop 0
	s_nop 0
	s_nop 0
	s_nop 0
	s_nop 0
	s_endpgm
